# speedup vs baseline: 1.0232x; 1.0130x over previous
_Z6gat_k1PKfS0_S0_S0_PDF16_S1_S1_Pf:
	s_load_dwordx8 s[4:11], s[0:1], 0x0
	s_load_dwordx8 s[12:19], s[0:1], 0x20
	v_lshrrev_b32_e32 v54, 6, v0
	v_and_b32_e32 v57, 0xc0, v0
	s_lshl_b32 s3, s2, 5
	v_and_b32_e32 v1, 63, v0
	v_bfe_u32 v55, v0, 5, 1
	v_lshlrev_b32_e32 v2, 8, v57
	v_mov_b32_e32 v19, 0
	v_or_b32_e32 v4, s3, v54
	v_and_b32_e32 v56, 31, v0
	v_lshl_or_b32 v18, v55, 11, v2
	v_lshlrev_b32_e32 v20, 4, v1
	v_mov_b32_e32 v21, v19
	v_ashrrev_i32_e32 v5, 31, v4
	s_waitcnt lgkmcnt(0)
	v_lshl_add_u64 v[2:3], s[6:7], 0, v[18:19]
	v_lshlrev_b32_e32 v18, 2, v56
	v_lshl_add_u64 v[6:7], s[4:5], 0, v[20:21]
	v_lshlrev_b64 v[8:9], 10, v[4:5]
	v_lshl_add_u64 v[2:3], v[2:3], 0, v[18:19]
	v_lshl_add_u64 v[10:11], v[6:7], 0, v[8:9]
	v_or_b32_e32 v12, 0x1000, v8
	v_mov_b32_e32 v13, v9
	global_load_dword v58, v[2:3], off
	global_load_dword v59, v[2:3], off offset:128
	global_load_dword v60, v[2:3], off offset:256
	global_load_dword v61, v[2:3], off offset:384
	global_load_dword v62, v[2:3], off offset:512
	global_load_dword v63, v[2:3], off offset:640
	global_load_dword v64, v[2:3], off offset:768
	global_load_dword v65, v[2:3], off offset:896
	v_lshl_add_u64 v[12:13], v[6:7], 0, v[12:13]
	global_load_dwordx4 v[22:25], v[10:11], off nt
	global_load_dwordx4 v[26:29], v[12:13], off nt
	v_or_b32_e32 v10, 0x2000, v8
	v_mov_b32_e32 v11, v9
	v_or_b32_e32 v8, 0x3000, v8
	v_lshl_add_u64 v[10:11], v[6:7], 0, v[10:11]
	v_lshl_add_u64 v[8:9], v[6:7], 0, v[8:9]
	global_load_dwordx4 v[30:33], v[10:11], off nt
	global_load_dwordx4 v[34:37], v[8:9], off nt
	v_or_b32_e32 v8, 16, v4
	v_ashrrev_i32_e32 v9, 31, v8
	v_or_b32_e32 v10, 20, v4
	v_lshlrev_b64 v[8:9], 10, v[8:9]
	v_ashrrev_i32_e32 v11, 31, v10
	v_lshl_add_u64 v[8:9], v[6:7], 0, v[8:9]
	v_lshlrev_b64 v[10:11], 10, v[10:11]
	v_lshl_add_u64 v[10:11], v[6:7], 0, v[10:11]
	global_load_dwordx4 v[38:41], v[8:9], off nt
	global_load_dwordx4 v[42:45], v[10:11], off nt
	v_or_b32_e32 v8, 24, v4
	v_ashrrev_i32_e32 v9, 31, v8
	v_or_b32_e32 v4, 28, v4
	v_lshlrev_b64 v[8:9], 10, v[8:9]
	v_ashrrev_i32_e32 v5, 31, v4
	v_lshl_add_u64 v[8:9], v[6:7], 0, v[8:9]
	v_lshlrev_b64 v[4:5], 10, v[4:5]
	v_lshl_add_u64 v[4:5], v[6:7], 0, v[4:5]
	global_load_dwordx4 v[46:49], v[8:9], off nt
	global_load_dwordx4 v[50:53], v[4:5], off nt
	global_load_dword v19, v[2:3], off offset:1024
	global_load_dword v66, v[2:3], off offset:1152
	global_load_dword v67, v[2:3], off offset:1280
	global_load_dword v68, v[2:3], off offset:1408
	global_load_dword v69, v[2:3], off offset:1536
	global_load_dword v70, v[2:3], off offset:1664
	global_load_dword v71, v[2:3], off offset:1792
	global_load_dword v72, v[2:3], off offset:1920
	s_movk_i32 s4, 0x1000
	v_add_co_u32_e32 v4, vcc, s4, v2
	s_movk_i32 s4, 0x2000
	s_nop 0
	v_addc_co_u32_e32 v5, vcc, 0, v3, vcc
	v_add_co_u32_e32 v6, vcc, s4, v2
	s_movk_i32 s4, 0x3000
	s_nop 0
	v_addc_co_u32_e32 v7, vcc, 0, v3, vcc
	global_load_dword v73, v[4:5], off offset:128
	global_load_dword v74, v[4:5], off offset:256
	global_load_dword v75, v[4:5], off offset:384
	global_load_dword v76, v[4:5], off offset:512
	global_load_dword v77, v[4:5], off offset:640
	global_load_dword v78, v[4:5], off offset:768
	global_load_dword v79, v[4:5], off offset:896
	global_load_dword v80, v[4:5], off offset:1024
	global_load_dword v81, v[4:5], off offset:1152
	global_load_dword v82, v[4:5], off offset:1280
	global_load_dword v83, v[4:5], off offset:1408
	global_load_dword v84, v[4:5], off offset:1536
	global_load_dword v85, v[4:5], off offset:1664
	global_load_dword v86, v[4:5], off offset:1792
	global_load_dword v87, v[4:5], off offset:1920
	global_load_dword v88, v[6:7], off offset:-4096
	global_load_dword v89, v[6:7], off
	global_load_dword v90, v[6:7], off offset:128
	global_load_dword v91, v[6:7], off offset:256
	global_load_dword v92, v[6:7], off offset:384
	global_load_dword v93, v[6:7], off offset:512
	global_load_dword v94, v[6:7], off offset:640
	global_load_dword v95, v[6:7], off offset:768
	global_load_dword v96, v[6:7], off offset:896
	global_load_dword v97, v[6:7], off offset:1024
	global_load_dword v98, v[6:7], off offset:1152
	global_load_dword v99, v[6:7], off offset:1280
	global_load_dword v100, v[6:7], off offset:1408
	global_load_dword v101, v[6:7], off offset:1536
	global_load_dword v102, v[6:7], off offset:1664
	global_load_dword v103, v[6:7], off offset:1792
	global_load_dword v104, v[6:7], off offset:1920
	v_add_co_u32_e32 v2, vcc, s4, v2
	v_and_b32_e32 v1, 7, v0
	s_nop 0
	v_addc_co_u32_e32 v3, vcc, 0, v3, vcc
	global_load_dword v105, v[2:3], off
	global_load_dword v106, v[2:3], off offset:128
	global_load_dword v107, v[2:3], off offset:256
	global_load_dword v108, v[2:3], off offset:384
	global_load_dword v109, v[2:3], off offset:512
	global_load_dword v110, v[2:3], off offset:640
	global_load_dword v111, v[2:3], off offset:768
	global_load_dword v112, v[2:3], off offset:896
	global_load_dword v113, v[2:3], off offset:1024
	global_load_dword v114, v[2:3], off offset:1152
	global_load_dword v115, v[2:3], off offset:1280
	global_load_dword v116, v[2:3], off offset:1408
	global_load_dword v117, v[2:3], off offset:1536
	global_load_dword v118, v[2:3], off offset:1664
	global_load_dword v119, v[2:3], off offset:1792
	global_load_dword v120, v[2:3], off offset:1920
	v_lshlrev_b32_e32 v121, 5, v1
	global_load_dwordx4 v[6:9], v121, s[8:9]
	global_load_dwordx4 v[2:5], v121, s[10:11]
	global_load_dwordx4 v[14:17], v121, s[8:9] offset:16
	global_load_dwordx4 v[10:13], v121, s[10:11] offset:16
	s_movk_i32 s4, 0x410
	v_mad_u32_u24 v122, v54, s4, v20
	s_movk_i32 s8, 0x110
	s_waitcnt vmcnt(62)
	ds_write_b128 v122, v[22:25] offset:34816
	ds_write_b128 v122, v[26:29] offset:38976
	ds_write_b128 v122, v[30:33] offset:43136
	ds_write_b128 v122, v[34:37] offset:47296
	ds_write_b128 v122, v[38:41] offset:51456
	ds_write_b128 v122, v[42:45] offset:55616
	s_waitcnt vmcnt(61)
	ds_write_b128 v122, v[46:49] offset:59776
	s_waitcnt vmcnt(60)
	ds_write_b128 v122, v[50:53] offset:63936
	v_mul_u32_u24_e32 v22, 0x410, v56
	v_lshlrev_b32_e32 v23, 2, v57
	v_and_b32_e32 v24, 32, v0
	v_add3_u32 v38, v22, v23, v24
	s_waitcnt lgkmcnt(0)
	s_barrier
	ds_read_b128 v[22:25], v38 offset:34832
	ds_read_b128 v[26:29], v38 offset:34816
	ds_read_b128 v[30:33], v38 offset:34880
	ds_read_b128 v[34:37], v38 offset:34896
	s_waitcnt lgkmcnt(3)
	v_cvt_pk_f16_f32 v25, v24, v25
	v_cvt_pk_f16_f32 v24, v22, v23
	s_waitcnt lgkmcnt(2)
	v_cvt_pk_f16_f32 v23, v28, v29
	v_cvt_pk_f16_f32 v22, v26, v27
	s_waitcnt vmcnt(53)
	v_cvt_pk_f16_f32 v29, v69, v71
	v_cvt_pk_f16_f32 v28, v19, v67
	v_cvt_pk_f16_f32 v27, v62, v64
	v_cvt_pk_f16_f32 v26, v58, v60
	v_lshlrev_b32_e32 v19, 2, v55
	s_nop 0
	v_mfma_f32_32x32x16_f16 a[0:15], v[22:25], v[26:29], 0
	s_waitcnt vmcnt(52)
	v_cvt_pk_f16_f32 v29, v70, v72
	v_cvt_pk_f16_f32 v28, v66, v68
	v_cvt_pk_f16_f32 v27, v63, v65
	v_cvt_pk_f16_f32 v26, v59, v61
	s_nop 1
	v_mfma_f32_32x32x16_f16 a[16:31], v[22:25], v[26:29], 0
	s_waitcnt lgkmcnt(0)
	v_cvt_pk_f16_f32 v25, v36, v37
	v_cvt_pk_f16_f32 v24, v34, v35
	v_cvt_pk_f16_f32 v23, v32, v33
	v_cvt_pk_f16_f32 v22, v30, v31
	ds_read_b128 v[30:33], v38 offset:34944
	ds_read_b128 v[34:37], v38 offset:34960
	s_waitcnt vmcnt(38)
	v_cvt_pk_f16_f32 v29, v84, v86
	v_cvt_pk_f16_f32 v28, v80, v82
	v_cvt_pk_f16_f32 v27, v76, v78
	s_waitcnt vmcnt(36)
	v_cvt_pk_f16_f32 v26, v88, v74
	s_nop 1
	v_mfma_f32_32x32x16_f16 a[0:15], v[22:25], v[26:29], a[0:15]
	v_cvt_pk_f16_f32 v29, v85, v87
	v_cvt_pk_f16_f32 v28, v81, v83
	v_cvt_pk_f16_f32 v27, v77, v79
	v_cvt_pk_f16_f32 v26, v73, v75
	s_nop 1
	v_mfma_f32_32x32x16_f16 a[16:31], v[22:25], v[26:29], a[16:31]
	s_waitcnt lgkmcnt(0)
	v_cvt_pk_f16_f32 v25, v36, v37
	v_cvt_pk_f16_f32 v24, v34, v35
	v_cvt_pk_f16_f32 v23, v32, v33
	v_cvt_pk_f16_f32 v22, v30, v31
	ds_read_b128 v[30:33], v38 offset:35008
	ds_read_b128 v[34:37], v38 offset:35024
	s_waitcnt vmcnt(21)
	v_cvt_pk_f16_f32 v29, v101, v103
	v_cvt_pk_f16_f32 v28, v97, v99
	v_cvt_pk_f16_f32 v27, v93, v95
	v_cvt_pk_f16_f32 v26, v89, v91
	s_nop 1
	v_mfma_f32_32x32x16_f16 a[0:15], v[22:25], v[26:29], a[0:15]
	s_waitcnt vmcnt(20)
	v_cvt_pk_f16_f32 v29, v102, v104
	v_cvt_pk_f16_f32 v28, v98, v100
	v_cvt_pk_f16_f32 v27, v94, v96
	v_cvt_pk_f16_f32 v26, v90, v92
	s_nop 1
	v_mfma_f32_32x32x16_f16 a[16:31], v[22:25], v[26:29], a[16:31]
	s_waitcnt lgkmcnt(0)
	v_cvt_pk_f16_f32 v25, v36, v37
	v_cvt_pk_f16_f32 v24, v34, v35
	v_cvt_pk_f16_f32 v23, v32, v33
	v_cvt_pk_f16_f32 v22, v30, v31
	s_waitcnt vmcnt(5)
	v_cvt_pk_f16_f32 v29, v117, v119
	v_cvt_pk_f16_f32 v28, v113, v115
	v_cvt_pk_f16_f32 v27, v109, v111
	v_cvt_pk_f16_f32 v26, v105, v107
	s_nop 1
	v_mfma_f32_32x32x16_f16 a[0:15], v[22:25], v[26:29], a[0:15]
	s_waitcnt vmcnt(4)
	v_cvt_pk_f16_f32 v29, v118, v120
	v_cvt_pk_f16_f32 v28, v114, v116
	v_cvt_pk_f16_f32 v27, v110, v112
	v_cvt_pk_f16_f32 v26, v106, v108
	s_nop 1
	v_mfma_f32_32x32x16_f16 a[16:31], v[22:25], v[26:29], a[16:31]
	v_lshl_or_b32 v22, v54, 5, v19
	v_mul_u32_u24_e32 v22, 0x44, v22
	v_lshl_add_u32 v22, v22, 2, v18
	s_nop 0
	ds_write_b32 v22, a0
	s_nop 6
	ds_write_b32 v22, a16 offset:128
	ds_write_b32 v22, a1 offset:272
	ds_write_b32 v22, a17 offset:400
	ds_write_b32 v22, a2 offset:544
	ds_write_b32 v22, a18 offset:672
	ds_write_b32 v22, a3 offset:816
	ds_write_b32 v22, a19 offset:944
	ds_write_b32 v22, a4 offset:2176
	ds_write_b32 v22, a20 offset:2304
	ds_write_b32 v22, a5 offset:2448
	ds_write_b32 v22, a21 offset:2576
	ds_write_b32 v22, a6 offset:2720
	ds_write_b32 v22, a22 offset:2848
	ds_write_b32 v22, a7 offset:2992
	ds_write_b32 v22, a23 offset:3120
	ds_write_b32 v22, a8 offset:4352
	ds_write_b32 v22, a24 offset:4480
	ds_write_b32 v22, a9 offset:4624
	ds_write_b32 v22, a25 offset:4752
	ds_write_b32 v22, a10 offset:4896
	ds_write_b32 v22, a26 offset:5024
	ds_write_b32 v22, a11 offset:5168
	ds_write_b32 v22, a27 offset:5296
	ds_write_b32 v22, a12 offset:6528
	ds_write_b32 v22, a28 offset:6656
	ds_write_b32 v22, a13 offset:6800
	ds_write_b32 v22, a29 offset:6928
	ds_write_b32 v22, a14 offset:7072
	ds_write_b32 v22, a30 offset:7200
	ds_write_b32 v22, a15 offset:7344
	ds_write_b32 v22, a31 offset:7472
	v_lshrrev_b32_e32 v22, 3, v0
	v_mad_u32_u24 v23, v22, s8, v121
	s_waitcnt lgkmcnt(0)
	s_barrier
	ds_read_b128 v[24:27], v23
	ds_read_b128 v[28:31], v23 offset:16
	ds_read_b128 v[32:35], v23 offset:8704
	s_waitcnt lgkmcnt(2)
	v_pk_add_f32 v[36:37], v[26:27], 0 op_sel_hi:[1,0]
	v_pk_add_f32 v[38:39], v[24:25], 0 op_sel_hi:[1,0]
	ds_read_b128 v[24:27], v23 offset:8720
	s_waitcnt lgkmcnt(2)
	v_pk_add_f32 v[40:41], v[30:31], 0 op_sel_hi:[1,0]
	v_pk_add_f32 v[42:43], v[28:29], 0 op_sel_hi:[1,0]
	ds_read_b128 v[28:31], v23 offset:17408
	s_waitcnt lgkmcnt(2)
	v_pk_add_f32 v[34:35], v[36:37], v[34:35]
	v_pk_add_f32 v[36:37], v[38:39], v[32:33]
	s_waitcnt lgkmcnt(1)
	v_pk_add_f32 v[38:39], v[40:41], v[26:27]
	v_pk_add_f32 v[40:41], v[42:43], v[24:25]
	ds_read_b128 v[24:27], v23 offset:17424
	s_waitcnt lgkmcnt(1)
	v_pk_add_f32 v[42:43], v[34:35], v[30:31]
	ds_read_b128 v[30:33], v23 offset:26112
	v_pk_add_f32 v[28:29], v[36:37], v[28:29]
	ds_read_b128 v[34:37], v23 offset:26128
	s_waitcnt lgkmcnt(2)
	v_pk_add_f32 v[40:41], v[40:41], v[24:25]
	v_pk_add_f32 v[38:39], v[38:39], v[26:27]
	s_waitcnt lgkmcnt(1)
	v_pk_add_f32 v[24:25], v[28:29], v[30:31]
	v_pk_add_f32 v[26:27], v[42:43], v[32:33]
	s_waitcnt lgkmcnt(0)
	v_pk_add_f32 v[28:29], v[40:41], v[34:35]
	v_pk_add_f32 v[30:31], v[38:39], v[36:37]
	s_waitcnt vmcnt(0)
	v_mul_f32_e32 v10, v28, v10
	v_fmac_f32_e32 v10, v24, v2
	v_mul_f32_e32 v14, v28, v14
	v_add_f32_e32 v2, 0, v10
	v_mul_f32_e32 v10, v29, v15
	v_fmac_f32_e32 v14, v24, v6
	v_fmac_f32_e32 v10, v25, v7
	v_mul_f32_e32 v7, v29, v11
	v_add_f32_e32 v6, 0, v14
	v_fmac_f32_e32 v7, v25, v3
	v_mul_f32_e32 v3, v30, v16
	v_add_f32_e32 v6, v6, v10
	v_fmac_f32_e32 v3, v26, v8
	v_add_f32_e32 v3, v6, v3
	v_mul_f32_e32 v6, v30, v12
	v_fmac_f32_e32 v6, v26, v4
	v_mul_f32_e32 v4, v31, v17
	v_fmac_f32_e32 v4, v27, v9
	v_add_f32_e32 v2, v2, v7
	v_add_f32_e32 v3, v3, v4
	v_mul_f32_e32 v4, v31, v13
	v_add_f32_e32 v2, v2, v6
	v_fmac_f32_e32 v4, v27, v5
	v_add_f32_e32 v2, v2, v4
	ds_write_b128 v23, v[24:27]
	ds_write_b128 v23, v[28:31] offset:16
	s_nop 1
	v_add_f32_dpp v3, v3, v3 quad_perm:[1,0,3,2] row_mask:0xf bank_mask:0xf
	v_add_f32_dpp v6, v2, v2 quad_perm:[1,0,3,2] row_mask:0xf bank_mask:0xf
	s_nop 1
	v_add_f32_dpp v3, v3, v3 quad_perm:[2,3,0,1] row_mask:0xf bank_mask:0xf
	v_add_f32_dpp v6, v6, v6 quad_perm:[2,3,0,1] row_mask:0xf bank_mask:0xf
	s_nop 1
	v_add_f32_dpp v2, v3, v3 row_half_mirror row_mask:0xf bank_mask:0xf
	v_add_f32_dpp v3, v6, v6 row_half_mirror row_mask:0xf bank_mask:0xf
	v_cmp_eq_u32_e32 vcc, 0, v1
	s_and_saveexec_b64 s[6:7], vcc
	s_cbranch_execz .LBB0_2
	v_mul_f32_e32 v4, 0x3f7d70a4, v3
	v_mul_f32_e32 v4, 0x3fb8aa3b, v4
	v_mul_f32_e32 v3, 0x3c23d70a, v3
	v_exp_f32_e32 v4, v4
	v_mul_f32_e32 v3, 0x3fb8aa3b, v3
	v_exp_f32_e32 v3, v3
	v_lshlrev_b32_e32 v5, 2, v22
	v_or_b32_e32 v6, 0x10a80, v5
	v_mul_f32_e32 v2, 0xbf7d70a4, v2
	ds_write_b32 v6, v4
	v_or_b32_e32 v4, 0x10a00, v5
	v_mul_f32_e32 v2, 0x3fb8aa3b, v2
	ds_write_b32 v4, v3
	v_exp_f32_e32 v4, v2
	v_add_u32_e32 v2, s3, v22
	v_ashrrev_i32_e32 v3, 31, v2
	s_waitcnt lgkmcnt(0)
	v_lshl_add_u64 v[2:3], v[2:3], 2, s[18:19]
	global_store_dword v[2:3], v4, off sc1
.LBB0_2:
	s_or_b64 exec, exec, s[6:7]
	v_bfe_u32 v16, v0, 6, 1
	v_lshl_or_b32 v2, v16, 4, v19
	s_movk_i32 s6, 0x80
	v_and_or_b32 v3, v0, s6, v18
	v_lshlrev_b32_e32 v6, 2, v2
	v_mad_u32_u24 v12, v2, s8, v3
	v_or_b32_e32 v2, 0x10a00, v6
	s_waitcnt lgkmcnt(0)
	s_barrier
	ds_read2_b32 v[10:11], v12 offset1:68
	ds_read_b128 v[2:5], v2
	v_or_b32_e32 v6, 0x10a20, v6
	ds_read_b128 v[6:9], v6
	v_add_u32_e32 v14, 0x800, v12
	v_cmp_gt_u32_e32 vcc, 32, v0
	s_waitcnt lgkmcnt(1)
	v_pk_mul_f32 v[2:3], v[10:11], v[2:3]
	ds_read2_b32 v[10:11], v12 offset0:136 offset1:204
	ds_read2_b32 v[12:13], v14 offset0:32 offset1:100
	ds_read2_b32 v[14:15], v14 offset0:168 offset1:236
	v_cvt_pk_f16_f32 v2, v2, v3
	s_waitcnt lgkmcnt(2)
	v_pk_mul_f32 v[4:5], v[10:11], v[4:5]
	s_nop 0
	v_cvt_pk_f16_f32 v3, v4, v5
	s_waitcnt lgkmcnt(1)
	v_pk_mul_f32 v[4:5], v[12:13], v[6:7]
	s_waitcnt lgkmcnt(0)
	v_pk_mul_f32 v[6:7], v[14:15], v[8:9]
	v_cvt_pk_f16_f32 v4, v4, v5
	v_cvt_pk_f16_f32 v5, v6, v7
	v_lshlrev_b32_e32 v6, 2, v0
	v_and_b32_e32 v6, 0x200, v6
	v_lshl_add_u32 v6, s2, 1, v6
	v_or_b32_e32 v6, v6, v16
	v_ashrrev_i32_e32 v7, 31, v6
	v_lshlrev_b64 v[6:7], 10, v[6:7]
	v_lshl_add_u64 v[6:7], s[12:13], 0, v[6:7]
	v_lshl_add_u64 v[6:7], v[6:7], 0, v[20:21]
	global_store_dwordx4 v[6:7], v[2:5], off sc1
	s_and_saveexec_b64 s[4:5], vcc
	s_cbranch_execz .LBB0_4
	v_lshlrev_b32_e32 v4, 1, v0
	v_bfe_u32 v2, v0, 3, 1
	v_and_b32_e32 v4, 8, v4
	v_and_b32_e32 v3, 16, v0
	v_and_or_b32 v0, v0, 3, v4
	v_lshlrev_b32_e32 v4, 2, v2
	v_or3_b32 v0, v0, v4, v3
	v_lshlrev_b32_e32 v0, 2, v0
	v_or_b32_e32 v4, 0x10a80, v0
	v_or_b32_e32 v0, 0x10a00, v0
	ds_read_b32 v4, v4
	ds_read_b32 v5, v0
	v_lshl_or_b32 v0, v2, 3, s3
	v_or3_b32 v0, v0, v3, v1
	s_waitcnt lgkmcnt(0)
	v_cvt_f16_f32_e32 v4, v4
	v_cvt_f16_f32_e32 v5, v5
	v_ashrrev_i32_e32 v1, 31, v0
	v_lshlrev_b64 v[0:1], 1, v[0:1]
	v_lshl_add_u64 v[2:3], s[14:15], 0, v[0:1]
	v_lshl_add_u64 v[0:1], s[16:17], 0, v[0:1]
	global_store_short v[2:3], v4, off sc1
	global_store_short v[0:1], v5, off sc1
